# speedup vs baseline: 1.0204x; 1.0029x over previous
.LBB3_13:
	s_or_b64 exec, exec, s[4:5]
	v_mov_b32_e32 v172, 0
	v_ashrrev_i32_e32 v1, 2, v0
	v_and_b32_e32 v1, 0xffffffc0, v1
	v_add_u32_e32 v1, s8, v1
	v_lshrrev_b32_e32 v130, 2, v0
	v_and_or_b32 v156, v130, 12, v1
	v_ashrrev_i32_e32 v157, 31, v156
	v_lshl_add_u64 v[150:151], v[156:157], 2, s[2:3]
	v_lshrrev_b32_e32 v254, 8, v0
	v_bfe_u32 v255, v0, 4, 2
	v_lshlrev_b32_e32 v254, 8, v254
	v_lshl_add_u32 v254, v255, 4, v254
	v_add_u32_e32 v254, 0x20000, v254
	ds_read_b128 v[138:141], v254
	ds_read_b128 v[142:145], v254 offset:64
	v_and_b32_e32 v130, 15, v0
	v_and_b32_e32 v180, 1, v0
	v_lshrrev_b32_e32 v0, 1, v0
	v_and_b32_e32 v131, 0x60, v0
	s_movk_i32 s3, 0xff6e
	v_lshl_or_b32 v131, s33, 8, v131
	v_lshlrev_b32_e32 v0, 4, v180
	v_or_b32_e32 v181, v131, v130
	v_bitop3_b32 v158, v131, s3, v130 bitop3:0xc8
	v_or_b32_e32 v130, v0, v156
	v_or_b32_e32 v132, 1, v181
	v_or_b32_e32 v134, 16, v158
	v_or_b32_e32 v136, 17, v181
	v_ashrrev_i32_e32 v131, 31, v130
	v_ashrrev_i32_e32 v133, 31, v132
	v_ashrrev_i32_e32 v135, 31, v134
	v_ashrrev_i32_e32 v137, 31, v136
	v_lshl_add_u64 v[160:161], v[130:131], 2, s[0:1]
	v_lshlrev_b64 v[152:153], 12, v[132:133]
	v_lshlrev_b64 v[148:149], 12, v[134:135]
	v_lshlrev_b64 v[146:147], 12, v[136:137]
	ds_read_b128 v[130:133], v254 offset:128
	ds_read_b128 v[134:137], v254 offset:192
	ds_read_b128 v[184:187], v254 offset:576
	ds_read_b128 v[188:191], v254 offset:512
	ds_read_b128 v[192:195], v254 offset:640
	ds_read_b128 v[196:199], v254 offset:704
	s_mov_b32 s2, 0x34800000
	v_cmp_eq_u32_e32 vcc, 0, v180
	v_mov_b32_e32 v173, 0
	v_mov_b32_e32 v174, 0
	v_mov_b32_e32 v175, 0
	v_ashrrev_i32_e32 v159, 31, v158
	v_mov_b32_e32 v176, 0
	v_mov_b32_e32 v177, 0
	v_mov_b32_e32 v178, 0
	v_mov_b32_e32 v179, 0
	v_lshlrev_b64 v[154:155], 12, v[158:159]
	v_lshl_add_u64 v[162:163], v[160:161], 0, v[154:155]
	v_lshl_add_u64 v[164:165], v[160:161], 0, v[152:153]
	v_lshl_add_u64 v[166:167], v[160:161], 0, v[148:149]
	v_mov_b32_e32 v1, 0
	s_waitcnt vmcnt(0) lgkmcnt(0)
	v_pk_fma_f32 v[128:129], v[128:129], s[2:3], v[140:141] op_sel_hi:[1,0,1]
	v_pk_fma_f32 v[126:127], v[126:127], s[2:3], v[138:139] op_sel_hi:[1,0,1]
	v_pk_fma_f32 v[120:121], v[120:121], s[2:3], v[144:145] op_sel_hi:[1,0,1]
	v_pk_fma_f32 v[118:119], v[118:119], s[2:3], v[142:143] op_sel_hi:[1,0,1]
	v_pk_fma_f32 v[124:125], v[124:125], s[2:3], v[140:141] op_sel_hi:[1,0,1]
	v_pk_fma_f32 v[122:123], v[122:123], s[2:3], v[138:139] op_sel_hi:[1,0,1]
	v_pk_fma_f32 v[168:169], v[116:117], s[2:3], v[144:145] op_sel_hi:[1,0,1]
	v_pk_fma_f32 v[170:171], v[114:115], s[2:3], v[142:143] op_sel_hi:[1,0,1]
	v_cndmask_b32_e32 v114, v129, v121, vcc
	v_cndmask_b32_e32 v115, v128, v120, vcc
	v_cndmask_b32_e32 v116, v127, v119, vcc
	v_cndmask_b32_e32 v117, v126, v118, vcc
	v_cndmask_b32_e32 v159, v125, v169, vcc
	v_cndmask_b32_e32 v180, v124, v168, vcc
	v_cndmask_b32_e32 v182, v123, v171, vcc
	v_cndmask_b32_e32 v183, v122, v170, vcc
	v_mov_b32_dpp v172, v117 quad_perm:[1,0,3,2] row_mask:0xf bank_mask:0xf
	v_mov_b32_dpp v173, v116 quad_perm:[1,0,3,2] row_mask:0xf bank_mask:0xf
	v_mov_b32_dpp v174, v115 quad_perm:[1,0,3,2] row_mask:0xf bank_mask:0xf
	v_mov_b32_dpp v175, v114 quad_perm:[1,0,3,2] row_mask:0xf bank_mask:0xf
	v_mov_b32_dpp v176, v183 quad_perm:[1,0,3,2] row_mask:0xf bank_mask:0xf
	v_mov_b32_dpp v177, v182 quad_perm:[1,0,3,2] row_mask:0xf bank_mask:0xf
	v_mov_b32_dpp v178, v180 quad_perm:[1,0,3,2] row_mask:0xf bank_mask:0xf
	v_mov_b32_dpp v179, v159 quad_perm:[1,0,3,2] row_mask:0xf bank_mask:0xf
	v_cndmask_b32_e32 v117, v175, v129, vcc
	v_cndmask_b32_e32 v116, v174, v128, vcc
	v_cndmask_b32_e32 v115, v173, v127, vcc
	v_cndmask_b32_e32 v114, v172, v126, vcc
	v_cndmask_b32_e32 v119, v119, v173, vcc
	v_pk_fma_f32 v[110:111], v[110:111], s[2:3], v[138:139] op_sel_hi:[1,0,1]
	v_pk_fma_f32 v[106:107], v[106:107], s[2:3], v[142:143] op_sel_hi:[1,0,1]
	v_cndmask_b32_e32 v121, v121, v175, vcc
	v_cndmask_b32_e32 v120, v120, v174, vcc
	v_cndmask_b32_e32 v118, v118, v172, vcc
	v_cndmask_b32_e32 v125, v179, v125, vcc
	v_cndmask_b32_e32 v124, v178, v124, vcc
	v_cndmask_b32_e32 v123, v177, v123, vcc
	v_cndmask_b32_e32 v122, v176, v122, vcc
	v_cndmask_b32_e32 v129, v169, v179, vcc
	v_cndmask_b32_e32 v128, v168, v178, vcc
	v_cndmask_b32_e32 v127, v171, v177, vcc
	v_cndmask_b32_e32 v126, v170, v176, vcc
	global_store_dwordx4 v[162:163], v[114:117], off sc0 sc1
	global_store_dwordx4 v[164:165], v[118:121], off sc0 sc1
	global_store_dwordx4 v[166:167], v[122:125], off sc0 sc1
	v_lshl_add_u64 v[114:115], v[160:161], 0, v[146:147]
	v_pk_fma_f32 v[112:113], v[112:113], s[2:3], v[140:141] op_sel_hi:[1,0,1]
	v_pk_fma_f32 v[108:109], v[108:109], s[2:3], v[144:145] op_sel_hi:[1,0,1]
	v_cndmask_b32_e32 v116, v111, v107, vcc
	v_mov_b32_e32 v119, 0
	global_store_dwordx4 v[114:115], v[126:129], off sc0 sc1
	v_cndmask_b32_e32 v115, v112, v108, vcc
	v_cndmask_b32_e32 v117, v110, v106, vcc
	v_mov_b32_e32 v118, 0
	v_mov_b32_dpp v119, v116 quad_perm:[1,0,3,2] row_mask:0xf bank_mask:0xf
	v_mov_b32_e32 v116, 0
	v_cndmask_b32_e32 v114, v113, v109, vcc
	v_mov_b32_dpp v118, v117 quad_perm:[1,0,3,2] row_mask:0xf bank_mask:0xf
	v_mov_b32_dpp v116, v115 quad_perm:[1,0,3,2] row_mask:0xf bank_mask:0xf
	v_mov_b32_e32 v115, 0
	v_cndmask_b32_e32 v112, v116, v112, vcc
	v_cndmask_b32_e32 v116, v108, v116, vcc
	v_mov_b32_dpp v115, v114 quad_perm:[1,0,3,2] row_mask:0xf bank_mask:0xf
	v_cndmask_b32_e32 v114, v106, v118, vcc
	v_or_b32_e32 v106, 0x80, v158
	v_cndmask_b32_e32 v113, v115, v113, vcc
	v_cndmask_b32_e32 v117, v109, v115, vcc
	v_cndmask_b32_e32 v115, v107, v119, vcc
	v_ashrrev_i32_e32 v107, 31, v106
	v_lshlrev_b64 v[108:109], 12, v[106:107]
	v_cndmask_b32_e32 v111, v119, v111, vcc
	v_cndmask_b32_e32 v110, v118, v110, vcc
	v_lshl_add_u64 v[106:107], v[160:161], 0, v[108:109]
	global_store_dwordx4 v[106:107], v[110:113], off sc0 sc1
	v_or_b32_e32 v106, 0x81, v181
	v_ashrrev_i32_e32 v107, 31, v106
	v_lshlrev_b64 v[106:107], 12, v[106:107]
	v_lshl_add_u64 v[110:111], v[160:161], 0, v[106:107]
	v_pk_fma_f32 v[102:103], v[102:103], s[2:3], v[138:139] op_sel_hi:[1,0,1]
	v_pk_fma_f32 v[98:99], v[98:99], s[2:3], v[142:143] op_sel_hi:[1,0,1]
	global_store_dwordx4 v[110:111], v[114:117], off sc0 sc1
	v_pk_fma_f32 v[104:105], v[104:105], s[2:3], v[140:141] op_sel_hi:[1,0,1]
	v_pk_fma_f32 v[100:101], v[100:101], s[2:3], v[144:145] op_sel_hi:[1,0,1]
	v_cndmask_b32_e32 v112, v103, v99, vcc
	v_mov_b32_e32 v115, 0
	v_cndmask_b32_e32 v111, v104, v100, vcc
	v_cndmask_b32_e32 v113, v102, v98, vcc
	v_mov_b32_e32 v114, 0
	v_mov_b32_dpp v115, v112 quad_perm:[1,0,3,2] row_mask:0xf bank_mask:0xf
	v_mov_b32_e32 v112, 0
	v_cndmask_b32_e32 v110, v105, v101, vcc
	v_mov_b32_dpp v114, v113 quad_perm:[1,0,3,2] row_mask:0xf bank_mask:0xf
	v_mov_b32_dpp v112, v111 quad_perm:[1,0,3,2] row_mask:0xf bank_mask:0xf
	v_mov_b32_e32 v111, 0
	v_cndmask_b32_e32 v104, v112, v104, vcc
	v_cndmask_b32_e32 v112, v100, v112, vcc
	v_mov_b32_dpp v111, v110 quad_perm:[1,0,3,2] row_mask:0xf bank_mask:0xf
	v_cndmask_b32_e32 v110, v98, v114, vcc
	v_or_b32_e32 v98, 0x90, v158
	v_cndmask_b32_e32 v105, v111, v105, vcc
	v_cndmask_b32_e32 v113, v101, v111, vcc
	v_cndmask_b32_e32 v111, v99, v115, vcc
	v_ashrrev_i32_e32 v99, 31, v98
	v_lshlrev_b64 v[100:101], 12, v[98:99]
	v_cndmask_b32_e32 v103, v115, v103, vcc
	v_cndmask_b32_e32 v102, v114, v102, vcc
	v_lshl_add_u64 v[98:99], v[160:161], 0, v[100:101]
	global_store_dwordx4 v[98:99], v[102:105], off sc0 sc1
	v_or_b32_e32 v98, 0x91, v181
	v_ashrrev_i32_e32 v99, 31, v98
	v_lshlrev_b64 v[98:99], 12, v[98:99]
	v_lshl_add_u64 v[102:103], v[160:161], 0, v[98:99]
	global_store_dwordx4 v[102:103], v[110:113], off sc0 sc1
	v_pk_fma_f32 v[96:97], v[96:97], s[2:3], v[132:133] op_sel_hi:[1,0,1]
	v_pk_fma_f32 v[94:95], v[94:95], s[2:3], v[130:131] op_sel_hi:[1,0,1]
	v_pk_fma_f32 v[104:105], v[92:93], s[2:3], v[136:137] op_sel_hi:[1,0,1]
	v_pk_fma_f32 v[110:111], v[90:91], s[2:3], v[134:135] op_sel_hi:[1,0,1]
	v_lshl_add_u64 v[102:103], v[0:1], 0, v[156:157]
	v_cndmask_b32_e32 v90, v97, v105, vcc
	v_cndmask_b32_e32 v91, v96, v104, vcc
	v_cndmask_b32_e32 v92, v95, v111, vcc
	v_cndmask_b32_e32 v93, v94, v110, vcc
	v_mov_b32_e32 v112, v1
	v_mov_b32_e32 v113, v1
	v_mov_b32_e32 v114, v1
	v_mov_b32_e32 v115, v1
	v_lshl_add_u64 v[102:103], v[102:103], 2, s[0:1]
	v_mov_b32_dpp v112, v93 quad_perm:[1,0,3,2] row_mask:0xf bank_mask:0xf
	v_mov_b32_dpp v113, v92 quad_perm:[1,0,3,2] row_mask:0xf bank_mask:0xf
	v_mov_b32_dpp v114, v91 quad_perm:[1,0,3,2] row_mask:0xf bank_mask:0xf
	v_mov_b32_dpp v115, v90 quad_perm:[1,0,3,2] row_mask:0xf bank_mask:0xf
	v_cndmask_b32_e32 v93, v115, v97, vcc
	v_cndmask_b32_e32 v92, v114, v96, vcc
	v_cndmask_b32_e32 v91, v113, v95, vcc
	v_cndmask_b32_e32 v90, v112, v94, vcc
	v_cndmask_b32_e32 v97, v105, v115, vcc
	v_cndmask_b32_e32 v96, v104, v114, vcc
	v_lshl_add_u64 v[104:105], v[102:103], 0, v[154:155]
	v_cndmask_b32_e32 v95, v111, v113, vcc
	v_cndmask_b32_e32 v94, v110, v112, vcc
	global_store_dwordx4 v[104:105], v[90:93], off offset:128 sc0 sc1
	v_pk_fma_f32 v[104:105], v[82:83], s[2:3], v[134:135] op_sel_hi:[1,0,1]
	v_mov_b32_e32 v111, v1
	v_lshl_add_u64 v[90:91], v[102:103], 0, v[152:153]
	global_store_dwordx4 v[90:91], v[94:97], off offset:128 sc0 sc1
	v_pk_fma_f32 v[90:91], v[88:89], s[2:3], v[132:133] op_sel_hi:[1,0,1]
	v_mov_b32_e32 v112, v1
	v_pk_fma_f32 v[94:95], v[86:87], s[2:3], v[130:131] op_sel_hi:[1,0,1]
	v_pk_fma_f32 v[96:97], v[84:85], s[2:3], v[136:137] op_sel_hi:[1,0,1]
	v_cndmask_b32_e32 v82, v94, v104, vcc
	s_nop 0
	v_cndmask_b32_e32 v110, v95, v105, vcc
	v_mov_b32_dpp v111, v82 quad_perm:[1,0,3,2] row_mask:0xf bank_mask:0xf
	s_nop 0
	v_cndmask_b32_e32 v92, v91, v97, vcc
	v_cndmask_b32_e32 v93, v90, v96, vcc
	v_mov_b32_dpp v112, v110 quad_perm:[1,0,3,2] row_mask:0xf bank_mask:0xf
	v_mov_b32_e32 v110, v1
	v_mov_b32_e32 v113, v1
	v_pk_fma_f32 v[80:81], v[80:81], s[2:3], v[132:133] op_sel_hi:[1,0,1]
	v_mov_b32_dpp v110, v93 quad_perm:[1,0,3,2] row_mask:0xf bank_mask:0xf
	v_mov_b32_dpp v113, v92 quad_perm:[1,0,3,2] row_mask:0xf bank_mask:0xf
	v_cndmask_b32_e32 v93, v113, v91, vcc
	v_cndmask_b32_e32 v92, v110, v90, vcc
	v_cndmask_b32_e32 v91, v112, v95, vcc
	v_cndmask_b32_e32 v90, v111, v94, vcc
	v_cndmask_b32_e32 v95, v105, v112, vcc
	v_cndmask_b32_e32 v94, v104, v111, vcc
	v_lshl_add_u64 v[104:105], v[102:103], 0, v[148:149]
	v_cndmask_b32_e32 v97, v97, v113, vcc
	v_cndmask_b32_e32 v96, v96, v110, vcc
	global_store_dwordx4 v[104:105], v[90:93], off offset:128 sc0 sc1
	v_pk_fma_f32 v[78:79], v[78:79], s[2:3], v[130:131] op_sel_hi:[1,0,1]
	v_pk_fma_f32 v[72:73], v[72:73], s[2:3], v[132:133] op_sel_hi:[1,0,1]
	v_lshl_add_u64 v[90:91], v[102:103], 0, v[146:147]
	global_store_dwordx4 v[90:91], v[94:97], off offset:128 sc0 sc1
	v_pk_fma_f32 v[90:91], v[76:77], s[2:3], v[136:137] op_sel_hi:[1,0,1]
	v_pk_fma_f32 v[92:93], v[74:75], s[2:3], v[134:135] op_sel_hi:[1,0,1]
	v_cndmask_b32_e32 v74, v81, v91, vcc
	v_cndmask_b32_e32 v75, v80, v90, vcc
	v_cndmask_b32_e32 v76, v79, v93, vcc
	v_cndmask_b32_e32 v77, v78, v92, vcc
	v_mov_b32_e32 v94, v1
	v_mov_b32_e32 v95, v1
	v_mov_b32_e32 v96, v1
	v_mov_b32_e32 v97, v1
	v_mov_b32_dpp v94, v77 quad_perm:[1,0,3,2] row_mask:0xf bank_mask:0xf
	v_mov_b32_dpp v95, v76 quad_perm:[1,0,3,2] row_mask:0xf bank_mask:0xf
	v_mov_b32_dpp v96, v75 quad_perm:[1,0,3,2] row_mask:0xf bank_mask:0xf
	v_mov_b32_dpp v97, v74 quad_perm:[1,0,3,2] row_mask:0xf bank_mask:0xf
	v_cndmask_b32_e32 v77, v97, v81, vcc
	v_cndmask_b32_e32 v76, v96, v80, vcc
	v_cndmask_b32_e32 v75, v95, v79, vcc
	v_cndmask_b32_e32 v74, v94, v78, vcc
	v_cndmask_b32_e32 v81, v91, v97, vcc
	v_cndmask_b32_e32 v80, v90, v96, vcc
	v_lshl_add_u64 v[90:91], v[102:103], 0, v[108:109]
	v_cndmask_b32_e32 v79, v93, v95, vcc
	v_cndmask_b32_e32 v78, v92, v94, vcc
	global_store_dwordx4 v[90:91], v[74:77], off offset:128 sc0 sc1
	v_pk_fma_f32 v[70:71], v[70:71], s[2:3], v[130:131] op_sel_hi:[1,0,1]
	s_nop 0
	v_pk_fma_f32 v[64:65], v[64:65], s[2:3], v[190:191] op_sel_hi:[1,0,1]
	v_lshl_add_u64 v[74:75], v[102:103], 0, v[106:107]
	global_store_dwordx4 v[74:75], v[78:81], off offset:128 sc0 sc1
	v_pk_fma_f32 v[74:75], v[68:69], s[2:3], v[136:137] op_sel_hi:[1,0,1]
	v_pk_fma_f32 v[76:77], v[66:67], s[2:3], v[134:135] op_sel_hi:[1,0,1]
	v_cndmask_b32_e32 v66, v73, v75, vcc
	v_cndmask_b32_e32 v67, v72, v74, vcc
	v_cndmask_b32_e32 v68, v71, v77, vcc
	v_cndmask_b32_e32 v69, v70, v76, vcc
	v_mov_b32_e32 v78, v1
	v_mov_b32_e32 v79, v1
	v_mov_b32_e32 v80, v1
	v_mov_b32_e32 v81, v1
	v_mov_b32_dpp v78, v69 quad_perm:[1,0,3,2] row_mask:0xf bank_mask:0xf
	v_mov_b32_dpp v79, v68 quad_perm:[1,0,3,2] row_mask:0xf bank_mask:0xf
	v_mov_b32_dpp v80, v67 quad_perm:[1,0,3,2] row_mask:0xf bank_mask:0xf
	v_mov_b32_dpp v81, v66 quad_perm:[1,0,3,2] row_mask:0xf bank_mask:0xf
	v_cndmask_b32_e32 v69, v81, v73, vcc
	v_cndmask_b32_e32 v68, v80, v72, vcc
	v_cndmask_b32_e32 v67, v79, v71, vcc
	v_cndmask_b32_e32 v66, v78, v70, vcc
	v_cndmask_b32_e32 v73, v75, v81, vcc
	v_cndmask_b32_e32 v72, v74, v80, vcc
	v_lshl_add_u64 v[74:75], v[102:103], 0, v[100:101]
	v_cndmask_b32_e32 v71, v77, v79, vcc
	v_cndmask_b32_e32 v70, v76, v78, vcc
	global_store_dwordx4 v[74:75], v[66:69], off offset:128 sc0 sc1
	v_pk_fma_f32 v[62:63], v[62:63], s[2:3], v[188:189] op_sel_hi:[1,0,1]
	v_mov_b32_e32 v74, v1
	v_lshl_add_u64 v[66:67], v[102:103], 0, v[98:99]
	global_store_dwordx4 v[66:67], v[70:73], off offset:128 sc0 sc1
	v_add_u32_e32 v66, 0x80, v156
	v_or_b32_e32 v68, v0, v66
	v_pk_fma_f32 v[70:71], v[60:61], s[2:3], v[186:187] op_sel_hi:[1,0,1]
	v_pk_fma_f32 v[72:73], v[58:59], s[2:3], v[184:185] op_sel_hi:[1,0,1]
	v_ashrrev_i32_e32 v69, 31, v68
	v_cndmask_b32_e32 v58, v65, v71, vcc
	v_cndmask_b32_e32 v59, v64, v70, vcc
	v_cndmask_b32_e32 v60, v63, v73, vcc
	v_cndmask_b32_e32 v61, v62, v72, vcc
	v_mov_b32_e32 v67, v1
	v_mov_b32_e32 v75, v1
	v_mov_b32_e32 v76, v1
	v_lshl_add_u64 v[68:69], v[68:69], 2, s[0:1]
	v_mov_b32_dpp v67, v61 quad_perm:[1,0,3,2] row_mask:0xf bank_mask:0xf
	v_mov_b32_dpp v74, v60 quad_perm:[1,0,3,2] row_mask:0xf bank_mask:0xf
	v_mov_b32_dpp v75, v59 quad_perm:[1,0,3,2] row_mask:0xf bank_mask:0xf
	v_mov_b32_dpp v76, v58 quad_perm:[1,0,3,2] row_mask:0xf bank_mask:0xf
	v_cndmask_b32_e32 v61, v76, v65, vcc
	v_cndmask_b32_e32 v60, v75, v64, vcc
	v_cndmask_b32_e32 v59, v74, v63, vcc
	v_cndmask_b32_e32 v58, v67, v62, vcc
	v_cndmask_b32_e32 v65, v71, v76, vcc
	v_cndmask_b32_e32 v64, v70, v75, vcc
	v_lshl_add_u64 v[70:71], v[68:69], 0, v[154:155]
	v_cndmask_b32_e32 v63, v73, v74, vcc
	v_cndmask_b32_e32 v62, v72, v67, vcc
	global_store_dwordx4 v[70:71], v[58:61], off sc0 sc1
	v_pk_fma_f32 v[70:71], v[50:51], s[2:3], v[184:185] op_sel_hi:[1,0,1]
	v_mov_b32_e32 v72, v1
	v_lshl_add_u64 v[58:59], v[68:69], 0, v[152:153]
	global_store_dwordx4 v[58:59], v[62:65], off sc0 sc1
	v_pk_fma_f32 v[58:59], v[56:57], s[2:3], v[190:191] op_sel_hi:[1,0,1]
	v_mov_b32_e32 v73, v1
	v_pk_fma_f32 v[62:63], v[54:55], s[2:3], v[188:189] op_sel_hi:[1,0,1]
	v_pk_fma_f32 v[64:65], v[52:53], s[2:3], v[186:187] op_sel_hi:[1,0,1]
	v_cndmask_b32_e32 v54, v62, v70, vcc
	s_nop 0
	v_cndmask_b32_e32 v67, v63, v71, vcc
	v_mov_b32_dpp v72, v54 quad_perm:[1,0,3,2] row_mask:0xf bank_mask:0xf
	s_nop 0
	v_cndmask_b32_e32 v60, v59, v65, vcc
	v_cndmask_b32_e32 v61, v58, v64, vcc
	v_mov_b32_dpp v73, v67 quad_perm:[1,0,3,2] row_mask:0xf bank_mask:0xf
	v_mov_b32_e32 v67, v1
	v_mov_b32_e32 v74, v1
	v_pk_fma_f32 v[48:49], v[48:49], s[2:3], v[190:191] op_sel_hi:[1,0,1]
	v_mov_b32_dpp v67, v61 quad_perm:[1,0,3,2] row_mask:0xf bank_mask:0xf
	v_mov_b32_dpp v74, v60 quad_perm:[1,0,3,2] row_mask:0xf bank_mask:0xf
	v_cndmask_b32_e32 v61, v74, v59, vcc
	v_cndmask_b32_e32 v60, v67, v58, vcc
	v_cndmask_b32_e32 v59, v73, v63, vcc
	v_cndmask_b32_e32 v58, v72, v62, vcc
	v_cndmask_b32_e32 v63, v71, v73, vcc
	v_cndmask_b32_e32 v62, v70, v72, vcc
	v_lshl_add_u64 v[70:71], v[68:69], 0, v[148:149]
	v_cndmask_b32_e32 v65, v65, v74, vcc
	v_cndmask_b32_e32 v64, v64, v67, vcc
	global_store_dwordx4 v[70:71], v[58:61], off sc0 sc1
	v_pk_fma_f32 v[46:47], v[46:47], s[2:3], v[188:189] op_sel_hi:[1,0,1]
	v_pk_fma_f32 v[40:41], v[40:41], s[2:3], v[190:191] op_sel_hi:[1,0,1]
	v_lshl_add_u64 v[58:59], v[68:69], 0, v[146:147]
	global_store_dwordx4 v[58:59], v[62:65], off sc0 sc1
	v_pk_fma_f32 v[58:59], v[44:45], s[2:3], v[186:187] op_sel_hi:[1,0,1]
	v_pk_fma_f32 v[60:61], v[42:43], s[2:3], v[184:185] op_sel_hi:[1,0,1]
	v_cndmask_b32_e32 v42, v49, v59, vcc
	v_cndmask_b32_e32 v43, v48, v58, vcc
	v_cndmask_b32_e32 v44, v47, v61, vcc
	v_cndmask_b32_e32 v45, v46, v60, vcc
	v_mov_b32_e32 v62, v1
	v_mov_b32_e32 v63, v1
	v_mov_b32_e32 v64, v1
	v_mov_b32_e32 v65, v1
	v_mov_b32_dpp v62, v45 quad_perm:[1,0,3,2] row_mask:0xf bank_mask:0xf
	v_mov_b32_dpp v63, v44 quad_perm:[1,0,3,2] row_mask:0xf bank_mask:0xf
	v_mov_b32_dpp v64, v43 quad_perm:[1,0,3,2] row_mask:0xf bank_mask:0xf
	v_mov_b32_dpp v65, v42 quad_perm:[1,0,3,2] row_mask:0xf bank_mask:0xf
	v_cndmask_b32_e32 v45, v65, v49, vcc
	v_cndmask_b32_e32 v44, v64, v48, vcc
	v_cndmask_b32_e32 v43, v63, v47, vcc
	v_cndmask_b32_e32 v42, v62, v46, vcc
	v_cndmask_b32_e32 v49, v59, v65, vcc
	v_cndmask_b32_e32 v48, v58, v64, vcc
	v_lshl_add_u64 v[58:59], v[68:69], 0, v[108:109]
	v_cndmask_b32_e32 v47, v61, v63, vcc
	v_cndmask_b32_e32 v46, v60, v62, vcc
	global_store_dwordx4 v[58:59], v[42:45], off sc0 sc1
	v_pk_fma_f32 v[38:39], v[38:39], s[2:3], v[188:189] op_sel_hi:[1,0,1]
	v_ashrrev_i32_e32 v67, 31, v66
	v_lshl_add_u64 v[42:43], v[68:69], 0, v[106:107]
	global_store_dwordx4 v[42:43], v[46:49], off sc0 sc1
	v_pk_fma_f32 v[42:43], v[32:33], s[2:3], v[186:187] op_sel_hi:[1,0,1]
	v_pk_fma_f32 v[44:45], v[30:31], s[2:3], v[184:185] op_sel_hi:[1,0,1]
	v_cndmask_b32_e32 v30, v41, v43, vcc
	v_cndmask_b32_e32 v31, v40, v42, vcc
	v_cndmask_b32_e32 v32, v39, v45, vcc
	v_cndmask_b32_e32 v33, v38, v44, vcc
	v_mov_b32_e32 v46, v1
	v_mov_b32_e32 v47, v1
	v_mov_b32_e32 v48, v1
	v_mov_b32_e32 v49, v1
	v_mov_b32_dpp v46, v33 quad_perm:[1,0,3,2] row_mask:0xf bank_mask:0xf
	v_mov_b32_dpp v47, v32 quad_perm:[1,0,3,2] row_mask:0xf bank_mask:0xf
	v_mov_b32_dpp v48, v31 quad_perm:[1,0,3,2] row_mask:0xf bank_mask:0xf
	v_mov_b32_dpp v49, v30 quad_perm:[1,0,3,2] row_mask:0xf bank_mask:0xf
	v_cndmask_b32_e32 v33, v49, v41, vcc
	v_cndmask_b32_e32 v32, v48, v40, vcc
	v_cndmask_b32_e32 v31, v47, v39, vcc
	v_cndmask_b32_e32 v30, v46, v38, vcc
	v_cndmask_b32_e32 v41, v43, v49, vcc
	v_cndmask_b32_e32 v40, v42, v48, vcc
	v_lshl_add_u64 v[42:43], v[68:69], 0, v[100:101]
	v_cndmask_b32_e32 v39, v45, v47, vcc
	v_cndmask_b32_e32 v38, v44, v46, vcc
	global_store_dwordx4 v[42:43], v[30:33], off sc0 sc1
	v_mov_b32_e32 v42, v1
	v_mov_b32_e32 v43, v1
	v_lshl_add_u64 v[30:31], v[68:69], 0, v[98:99]
	global_store_dwordx4 v[30:31], v[38:41], off sc0 sc1
	v_lshl_add_u64 v[30:31], v[0:1], 0, v[66:67]
	s_nop 0
	v_pk_fma_f32 v[32:33], v[34:35], s[2:3], v[192:193] op_sel_hi:[1,0,1]
	v_lshl_add_u64 v[38:39], v[30:31], 2, s[0:1]
	v_pk_fma_f32 v[30:31], v[36:37], s[2:3], v[194:195] op_sel_hi:[1,0,1]
	v_pk_fma_f32 v[34:35], v[28:29], s[2:3], v[198:199] op_sel_hi:[1,0,1]
	v_pk_fma_f32 v[36:37], v[26:27], s[2:3], v[196:197] op_sel_hi:[1,0,1]
	v_cndmask_b32_e32 v0, v31, v35, vcc
	v_cndmask_b32_e32 v26, v30, v34, vcc
	v_cndmask_b32_e32 v27, v33, v37, vcc
	v_cndmask_b32_e32 v28, v32, v36, vcc
	v_mov_b32_e32 v40, v1
	v_mov_b32_e32 v41, v1
	v_mov_b32_dpp v42, v26 quad_perm:[1,0,3,2] row_mask:0xf bank_mask:0xf
	v_mov_b32_dpp v40, v28 quad_perm:[1,0,3,2] row_mask:0xf bank_mask:0xf
	v_mov_b32_dpp v41, v27 quad_perm:[1,0,3,2] row_mask:0xf bank_mask:0xf
	v_mov_b32_dpp v43, v0 quad_perm:[1,0,3,2] row_mask:0xf bank_mask:0xf
	v_cndmask_b32_e32 v29, v43, v31, vcc
	v_cndmask_b32_e32 v28, v42, v30, vcc
	v_cndmask_b32_e32 v27, v41, v33, vcc
	v_cndmask_b32_e32 v26, v40, v32, vcc
	v_cndmask_b32_e32 v33, v35, v43, vcc
	v_cndmask_b32_e32 v32, v34, v42, vcc
	v_lshl_add_u64 v[34:35], v[38:39], 0, v[154:155]
	v_cndmask_b32_e32 v31, v37, v41, vcc
	v_cndmask_b32_e32 v30, v36, v40, vcc
	global_store_dwordx4 v[34:35], v[26:29], off offset:128 sc0 sc1
	v_pk_fma_f32 v[24:25], v[24:25], s[2:3], v[194:195] op_sel_hi:[1,0,1]
	v_pk_fma_f32 v[22:23], v[22:23], s[2:3], v[192:193] op_sel_hi:[1,0,1]
	v_lshl_add_u64 v[26:27], v[38:39], 0, v[152:153]
	global_store_dwordx4 v[26:27], v[30:33], off offset:128 sc0 sc1
	v_pk_fma_f32 v[26:27], v[20:21], s[2:3], v[198:199] op_sel_hi:[1,0,1]
	v_pk_fma_f32 v[28:29], v[18:19], s[2:3], v[196:197] op_sel_hi:[1,0,1]
	v_cndmask_b32_e32 v0, v25, v27, vcc
	v_cndmask_b32_e32 v18, v24, v26, vcc
	v_cndmask_b32_e32 v19, v23, v29, vcc
	v_cndmask_b32_e32 v20, v22, v28, vcc
	v_mov_b32_e32 v30, v1
	v_mov_b32_e32 v31, v1
	v_mov_b32_e32 v32, v1
	v_mov_b32_e32 v33, v1
	v_mov_b32_dpp v30, v20 quad_perm:[1,0,3,2] row_mask:0xf bank_mask:0xf
	v_mov_b32_dpp v31, v19 quad_perm:[1,0,3,2] row_mask:0xf bank_mask:0xf
	v_mov_b32_dpp v32, v18 quad_perm:[1,0,3,2] row_mask:0xf bank_mask:0xf
	v_mov_b32_dpp v33, v0 quad_perm:[1,0,3,2] row_mask:0xf bank_mask:0xf
	v_cndmask_b32_e32 v21, v33, v25, vcc
	v_cndmask_b32_e32 v20, v32, v24, vcc
	v_cndmask_b32_e32 v19, v31, v23, vcc
	v_cndmask_b32_e32 v18, v30, v22, vcc
	v_cndmask_b32_e32 v25, v27, v33, vcc
	v_cndmask_b32_e32 v24, v26, v32, vcc
	v_lshl_add_u64 v[26:27], v[38:39], 0, v[148:149]
	v_cndmask_b32_e32 v23, v29, v31, vcc
	v_cndmask_b32_e32 v22, v28, v30, vcc
	global_store_dwordx4 v[26:27], v[18:21], off offset:128 sc0 sc1
	v_pk_fma_f32 v[16:17], v[16:17], s[2:3], v[194:195] op_sel_hi:[1,0,1]
	v_pk_fma_f32 v[14:15], v[14:15], s[2:3], v[192:193] op_sel_hi:[1,0,1]
	v_lshl_add_u64 v[18:19], v[38:39], 0, v[146:147]
	global_store_dwordx4 v[18:19], v[22:25], off offset:128 sc0 sc1
	v_pk_fma_f32 v[18:19], v[12:13], s[2:3], v[198:199] op_sel_hi:[1,0,1]
	v_pk_fma_f32 v[20:21], v[10:11], s[2:3], v[196:197] op_sel_hi:[1,0,1]
	v_cndmask_b32_e32 v0, v17, v19, vcc
	v_cndmask_b32_e32 v10, v16, v18, vcc
	v_cndmask_b32_e32 v11, v15, v21, vcc
	v_cndmask_b32_e32 v12, v14, v20, vcc
	v_mov_b32_e32 v22, v1
	v_mov_b32_e32 v23, v1
	v_mov_b32_e32 v24, v1
	v_mov_b32_e32 v25, v1
	v_mov_b32_dpp v22, v12 quad_perm:[1,0,3,2] row_mask:0xf bank_mask:0xf
	v_mov_b32_dpp v23, v11 quad_perm:[1,0,3,2] row_mask:0xf bank_mask:0xf
	v_mov_b32_dpp v24, v10 quad_perm:[1,0,3,2] row_mask:0xf bank_mask:0xf
	v_mov_b32_dpp v25, v0 quad_perm:[1,0,3,2] row_mask:0xf bank_mask:0xf
	v_cndmask_b32_e32 v13, v25, v17, vcc
	v_cndmask_b32_e32 v12, v24, v16, vcc
	v_cndmask_b32_e32 v11, v23, v15, vcc
	v_cndmask_b32_e32 v10, v22, v14, vcc
	v_cndmask_b32_e32 v17, v19, v25, vcc
	v_cndmask_b32_e32 v16, v18, v24, vcc
	v_lshl_add_u64 v[18:19], v[38:39], 0, v[108:109]
	v_cndmask_b32_e32 v15, v21, v23, vcc
	v_cndmask_b32_e32 v14, v20, v22, vcc
	global_store_dwordx4 v[18:19], v[10:13], off offset:128 sc0 sc1
	v_pk_fma_f32 v[8:9], v[8:9], s[2:3], v[194:195] op_sel_hi:[1,0,1]
	v_pk_fma_f32 v[6:7], v[6:7], s[2:3], v[192:193] op_sel_hi:[1,0,1]
	v_lshl_add_u64 v[10:11], v[38:39], 0, v[106:107]
	global_store_dwordx4 v[10:11], v[14:17], off offset:128 sc0 sc1
	v_pk_fma_f32 v[10:11], v[4:5], s[2:3], v[198:199] op_sel_hi:[1,0,1]
	v_pk_fma_f32 v[12:13], v[2:3], s[2:3], v[196:197] op_sel_hi:[1,0,1]
	v_cndmask_b32_e32 v0, v9, v11, vcc
	v_cndmask_b32_e32 v2, v8, v10, vcc
	v_cndmask_b32_e32 v3, v7, v13, vcc
	v_cndmask_b32_e32 v4, v6, v12, vcc
	v_mov_b32_e32 v14, v1
	v_mov_b32_e32 v15, v1
	v_mov_b32_e32 v16, v1
	v_mov_b32_dpp v14, v4 quad_perm:[1,0,3,2] row_mask:0xf bank_mask:0xf
	v_mov_b32_dpp v15, v3 quad_perm:[1,0,3,2] row_mask:0xf bank_mask:0xf
	v_mov_b32_dpp v16, v2 quad_perm:[1,0,3,2] row_mask:0xf bank_mask:0xf
	v_mov_b32_dpp v1, v0 quad_perm:[1,0,3,2] row_mask:0xf bank_mask:0xf
	v_cndmask_b32_e32 v5, v1, v9, vcc
	v_cndmask_b32_e32 v4, v16, v8, vcc
	v_cndmask_b32_e32 v3, v15, v7, vcc
	v_cndmask_b32_e32 v2, v14, v6, vcc
	v_cndmask_b32_e32 v9, v11, v1, vcc
	v_lshl_add_u64 v[0:1], v[38:39], 0, v[100:101]
	v_cndmask_b32_e32 v8, v10, v16, vcc
	v_cndmask_b32_e32 v7, v13, v15, vcc
	v_cndmask_b32_e32 v6, v12, v14, vcc
	global_store_dwordx4 v[0:1], v[2:5], off offset:128 sc0 sc1
	v_lshl_add_u64 v[0:1], v[38:39], 0, v[98:99]
	global_store_dwordx4 v[0:1], v[6:9], off offset:128 sc0 sc1
	s_endpgm
